# speedup vs baseline: 1.1049x; 1.0028x over previous
.LBB2_83:
	s_lshl_b32 s30, s18, 11
	s_mov_b32 s31, 0
	v_lshl_add_u64 v[252:253], v[122:123], 0, s[30:31]
	s_bitset1_b32 s30, 12
	v_lshl_add_u64 v[254:255], v[122:123], 0, s[30:31]
	global_load_dwordx4 v[240:243], v[254:255], off
	global_load_dwordx4 v[236:239], v[252:253], off
	global_load_dwordx4 v[244:247], v[252:253], off offset:1024
	global_load_dwordx4 v[248:251], v[254:255], off offset:1024
	s_lshl_b32 s24, s18, 6
	v_add3_u32 v184, v171, s24, v172
	ds_read_b128 v[38:41], v184
	ds_read_b128 v[42:45], v184 offset:4608
	v_lshl_or_b32 v183, s18, 5, v174
	v_mad_u32_u24 v183, v183, s15, v163
	s_waitcnt lgkmcnt(0)
	v_mfma_f32_32x32x16_f16 v[82:97], v[38:41], v[34:37], 0
	ds_read_b128 v[38:41], v184 offset:9216
	v_mfma_f32_32x32x16_f16 v[66:81], v[42:45], v[34:37], 0
	s_nop 9
	ds_read_b128 v[42:45], v184 offset:13824
	s_waitcnt lgkmcnt(0)
	v_mfma_f32_32x32x16_f16 v[50:65], v[38:41], v[34:37], 0
	v_mfma_f32_32x32x16_f16 v[34:49], v[42:45], v[34:37], 0
	s_nop 3
	s_nop 1
	v_exp_f32_e32 v66, v66
	v_exp_f32_e32 v67, v67
	v_exp_f32_e32 v68, v68
	v_exp_f32_e32 v69, v69
	v_cvt_pkrtz_f16_f32 v66, v66, v67
	v_cvt_pkrtz_f16_f32 v67, v68, v69
	v_exp_f32_e32 v68, v70
	v_exp_f32_e32 v69, v71
	v_exp_f32_e32 v70, v72
	v_exp_f32_e32 v71, v73
	v_cvt_pkrtz_f16_f32 v68, v68, v69
	v_cvt_pkrtz_f16_f32 v69, v70, v71
	v_exp_f32_e32 v70, v74
	v_exp_f32_e32 v71, v75
	v_exp_f32_e32 v72, v76
	v_exp_f32_e32 v73, v77
	v_cvt_pkrtz_f16_f32 v70, v70, v71
	v_cvt_pkrtz_f16_f32 v71, v72, v73
	v_exp_f32_e32 v50, v50
	v_exp_f32_e32 v51, v51
	v_exp_f32_e32 v72, v78
	v_exp_f32_e32 v73, v79
	v_exp_f32_e32 v74, v80
	v_exp_f32_e32 v75, v81
	v_exp_f32_e32 v52, v52
	v_exp_f32_e32 v53, v53
	v_cvt_pkrtz_f16_f32 v50, v50, v51
	v_cvt_pkrtz_f16_f32 v72, v72, v73
	v_cvt_pkrtz_f16_f32 v73, v74, v75
	v_and_b32_e32 v74, v143, v50
	v_cvt_pkrtz_f16_f32 v50, v52, v53
	v_and_b32_e32 v75, v144, v50
	v_exp_f32_e32 v50, v54
	v_exp_f32_e32 v51, v55
	v_exp_f32_e32 v52, v56
	v_exp_f32_e32 v53, v57
	v_cvt_pkrtz_f16_f32 v50, v50, v51
	v_and_b32_e32 v76, v145, v50
	v_cvt_pkrtz_f16_f32 v50, v52, v53
	v_and_b32_e32 v77, v146, v50
	v_exp_f32_e32 v50, v58
	v_exp_f32_e32 v51, v59
	v_exp_f32_e32 v52, v60
	v_exp_f32_e32 v53, v61
	v_exp_f32_e32 v82, v82
	v_exp_f32_e32 v83, v83
	v_exp_f32_e32 v84, v84
	v_exp_f32_e32 v85, v85
	v_cvt_pkrtz_f16_f32 v50, v50, v51
	v_and_b32_e32 v78, v147, v50
	v_cvt_pkrtz_f16_f32 v50, v52, v53
	v_cvt_pkrtz_f16_f32 v82, v82, v83
	v_cvt_pkrtz_f16_f32 v83, v84, v85
	v_exp_f32_e32 v84, v86
	v_exp_f32_e32 v85, v87
	v_and_b32_e32 v79, v148, v50
	v_exp_f32_e32 v86, v88
	v_exp_f32_e32 v87, v89
	v_exp_f32_e32 v50, v62
	v_exp_f32_e32 v51, v63
	v_exp_f32_e32 v52, v64
	v_exp_f32_e32 v53, v65
	v_cvt_pkrtz_f16_f32 v84, v84, v85
	v_cvt_pkrtz_f16_f32 v85, v86, v87
	v_cvt_pkrtz_f16_f32 v50, v50, v51
	v_exp_f32_e32 v86, v90
	v_exp_f32_e32 v87, v91
	v_exp_f32_e32 v88, v92
	v_exp_f32_e32 v89, v93
	v_and_b32_e32 v80, v149, v50
	v_cvt_pkrtz_f16_f32 v50, v52, v53
	v_and_b32_e32 v81, v150, v50
	ds_read_b128 v[50:53], v183
	v_cvt_pkrtz_f16_f32 v86, v86, v87
	v_cvt_pkrtz_f16_f32 v87, v88, v89
	v_exp_f32_e32 v88, v94
	v_exp_f32_e32 v89, v95
	v_exp_f32_e32 v90, v96
	v_exp_f32_e32 v91, v97
	v_exp_f32_e32 v34, v34
	v_exp_f32_e32 v35, v35
	v_exp_f32_e32 v36, v36
	v_exp_f32_e32 v37, v37
	v_and_b32_e32 v82, v127, v82
	v_and_b32_e32 v83, v128, v83
	v_and_b32_e32 v84, v129, v84
	v_and_b32_e32 v85, v130, v85
	v_cvt_pkrtz_f16_f32 v88, v88, v89
	v_cvt_pkrtz_f16_f32 v89, v90, v91
	ds_read_b128 v[90:93], v183 offset:32
	s_waitcnt lgkmcnt(0)
	v_mfma_f32_32x32x16_f16 v[50:65], v[50:53], v[82:85], 0
	v_cvt_pkrtz_f16_f32 v34, v34, v35
	v_cvt_pkrtz_f16_f32 v35, v36, v37
	v_exp_f32_e32 v36, v38
	v_exp_f32_e32 v37, v39
	v_exp_f32_e32 v38, v40
	v_exp_f32_e32 v39, v41
	v_and_b32_e32 v86, v131, v86
	v_and_b32_e32 v87, v132, v87
	v_and_b32_e32 v88, v133, v88
	v_and_b32_e32 v89, v134, v89
	v_cvt_pkrtz_f16_f32 v36, v36, v37
	v_cvt_pkrtz_f16_f32 v37, v38, v39
	ds_read_b128 v[38:41], v183 offset:64
	v_mfma_f32_32x32x16_f16 v[50:65], v[90:93], v[86:89], v[50:65]
	v_mov_b32_e32 v186, 0
	v_dot2c_f32_f16_e32 v186, 0x3c003c00, v82
	v_dot2c_f32_f16_e32 v186, 0x3c003c00, v83
	v_dot2c_f32_f16_e32 v186, 0x3c003c00, v84
	v_dot2c_f32_f16_e32 v186, 0x3c003c00, v85
	v_and_b32_e32 v66, v135, v66
	v_and_b32_e32 v67, v136, v67
	v_and_b32_e32 v68, v137, v68
	v_and_b32_e32 v69, v138, v69
	ds_read_b128 v[82:85], v183 offset:96
	s_waitcnt lgkmcnt(0)
	v_mfma_f32_32x32x16_f16 v[50:65], v[38:41], v[66:69], v[50:65]
	v_exp_f32_e32 v42, v42
	v_exp_f32_e32 v43, v43
	v_and_b32_e32 v70, v139, v70
	v_and_b32_e32 v71, v140, v71
	v_and_b32_e32 v72, v141, v72
	v_and_b32_e32 v73, v142, v73
	v_cvt_pkrtz_f16_f32 v38, v42, v43
	v_exp_f32_e32 v39, v44
	v_exp_f32_e32 v44, v45
	ds_read_b128 v[40:43], v183 offset:128
	v_dot2c_f32_f16_e32 v186, 0x3c003c00, v86
	v_mfma_f32_32x32x16_f16 v[50:65], v[82:85], v[70:73], v[50:65]
	v_dot2c_f32_f16_e32 v186, 0x3c003c00, v87
	v_dot2c_f32_f16_e32 v186, 0x3c003c00, v88
	v_dot2c_f32_f16_e32 v186, 0x3c003c00, v89
	v_dot2c_f32_f16_e32 v186, 0x3c003c00, v66
	v_dot2c_f32_f16_e32 v186, 0x3c003c00, v67
	v_dot2c_f32_f16_e32 v186, 0x3c003c00, v68
	v_dot2c_f32_f16_e32 v186, 0x3c003c00, v69
	ds_read_b128 v[66:69], v183 offset:160
	s_waitcnt lgkmcnt(0)
	v_mfma_f32_32x32x16_f16 v[50:65], v[40:43], v[74:77], v[50:65]
	v_dot2c_f32_f16_e32 v186, 0x3c003c00, v70
	v_dot2c_f32_f16_e32 v186, 0x3c003c00, v71
	v_dot2c_f32_f16_e32 v186, 0x3c003c00, v72
	v_cvt_pkrtz_f16_f32 v39, v39, v44
	v_dot2c_f32_f16_e32 v186, 0x3c003c00, v73
	v_exp_f32_e32 v46, v46
	v_exp_f32_e32 v40, v47
	v_exp_f32_e32 v47, v49
	ds_read_b128 v[42:45], v183 offset:192
	v_dot2c_f32_f16_e32 v186, 0x3c003c00, v74
	v_mfma_f32_32x32x16_f16 v[50:65], v[66:69], v[78:81], v[50:65]
	v_dot2c_f32_f16_e32 v186, 0x3c003c00, v75
	v_dot2c_f32_f16_e32 v186, 0x3c003c00, v76
	v_dot2c_f32_f16_e32 v186, 0x3c003c00, v77
	v_exp_f32_e32 v41, v48
	v_dot2c_f32_f16_e32 v186, 0x3c003c00, v78
	v_dot2c_f32_f16_e32 v186, 0x3c003c00, v79
	v_dot2c_f32_f16_e32 v186, 0x3c003c00, v80
	v_dot2c_f32_f16_e32 v186, 0x3c003c00, v81
	v_and_b32_e32 v34, v151, v34
	v_and_b32_e32 v35, v152, v35
	v_and_b32_e32 v36, v153, v36
	v_and_b32_e32 v37, v154, v37
	v_cvt_pkrtz_f16_f32 v40, v46, v40
	v_cvt_pkrtz_f16_f32 v41, v41, v47
	ds_read_b128 v[46:49], v183 offset:224
	v_dot2c_f32_f16_e32 v186, 0x3c003c00, v34
	s_waitcnt lgkmcnt(0)
	v_mfma_f32_32x32x16_f16 v[50:65], v[42:45], v[34:37], v[50:65]
	v_dot2c_f32_f16_e32 v186, 0x3c003c00, v35
	v_dot2c_f32_f16_e32 v186, 0x3c003c00, v36
	v_dot2c_f32_f16_e32 v186, 0x3c003c00, v37
	v_and_b32_e32 v38, v155, v38
	v_dot2c_f32_f16_e32 v186, 0x3c003c00, v38
	v_and_b32_e32 v39, v156, v39
	v_dot2c_f32_f16_e32 v186, 0x3c003c00, v39
	v_and_b32_e32 v40, v157, v40
	v_dot2c_f32_f16_e32 v186, 0x3c003c00, v40
	v_and_b32_e32 v41, v158, v41
	v_dot2c_f32_f16_e32 v186, 0x3c003c00, v41
	s_nop 0
	v_mfma_f32_32x32x16_f16 v[50:65], v[46:49], v[38:41], v[50:65]
	s_nop 0
	v_mov_b32_e32 v34, v186
	v_mov_b32_e32 v35, v186
	s_nop 1
	v_permlane32_swap_b32_e32 v34, v35
	v_cndmask_b32_e64 v34, v34, v35, s[2:3]
	v_add_f32_e32 v34, v186, v34
	v_rcp_f32_e32 v34, v34
	s_nop 2
	v_mul_f32_e32 v185, v34, v50
	v_mul_f32_e32 v186, v34, v51
	v_mul_f32_e32 v187, v34, v52
	v_mul_f32_e32 v188, v34, v53
	v_mul_f32_e32 v189, v34, v54
	v_mul_f32_e32 v190, v34, v55
	v_mul_f32_e32 v191, v34, v56
	v_mul_f32_e32 v192, v34, v57
	ds_read_b128 v[34:37], v184 offset:32
	s_waitcnt lgkmcnt(0)
	v_mfma_f32_32x32x16_f16 v[82:97], v[34:37], v[114:117], 0
	ds_read_b128 v[34:37], v184 offset:4640
	ds_read_b128 v[38:41], v184 offset:9248
	s_nop 9
	s_waitcnt lgkmcnt(0)
	v_mfma_f32_32x32x16_f16 v[66:81], v[34:37], v[114:117], 0
	ds_read_b128 v[34:37], v184 offset:13856
	v_mfma_f32_32x32x16_f16 v[50:65], v[38:41], v[114:117], 0
	s_nop 2
	s_waitcnt lgkmcnt(0)
	v_mfma_f32_32x32x16_f16 v[34:49], v[34:37], v[114:117], 0
	s_nop 1
	s_nop 1
	s_nop 0
	v_exp_f32_e32 v66, v66
	v_exp_f32_e32 v67, v67
	v_exp_f32_e32 v68, v68
	v_exp_f32_e32 v69, v69
	v_cvt_pkrtz_f16_f32 v66, v66, v67
	v_cvt_pkrtz_f16_f32 v67, v68, v69
	v_exp_f32_e32 v68, v70
	v_exp_f32_e32 v69, v71
	v_exp_f32_e32 v70, v72
	v_exp_f32_e32 v71, v73
	v_cvt_pkrtz_f16_f32 v68, v68, v69
	v_cvt_pkrtz_f16_f32 v69, v70, v71
	v_exp_f32_e32 v70, v74
	v_exp_f32_e32 v71, v75
	v_exp_f32_e32 v72, v76
	v_exp_f32_e32 v73, v77
	v_cvt_pkrtz_f16_f32 v70, v70, v71
	v_cvt_pkrtz_f16_f32 v71, v72, v73
	v_exp_f32_e32 v50, v50
	v_exp_f32_e32 v51, v51
	v_exp_f32_e32 v72, v78
	v_exp_f32_e32 v73, v79
	v_exp_f32_e32 v74, v80
	v_exp_f32_e32 v75, v81
	v_exp_f32_e32 v52, v52
	v_exp_f32_e32 v53, v53
	v_cvt_pkrtz_f16_f32 v50, v50, v51
	v_cvt_pkrtz_f16_f32 v72, v72, v73
	v_cvt_pkrtz_f16_f32 v73, v74, v75
	v_and_b32_e32 v74, v143, v50
	v_cvt_pkrtz_f16_f32 v50, v52, v53
	v_and_b32_e32 v75, v144, v50
	v_exp_f32_e32 v50, v54
	v_exp_f32_e32 v51, v55
	v_exp_f32_e32 v52, v56
	v_exp_f32_e32 v53, v57
	v_cvt_pkrtz_f16_f32 v50, v50, v51
	v_and_b32_e32 v76, v145, v50
	v_cvt_pkrtz_f16_f32 v50, v52, v53
	v_and_b32_e32 v77, v146, v50
	v_exp_f32_e32 v50, v58
	v_exp_f32_e32 v51, v59
	v_exp_f32_e32 v52, v60
	v_exp_f32_e32 v53, v61
	v_exp_f32_e32 v82, v82
	v_exp_f32_e32 v83, v83
	v_exp_f32_e32 v84, v84
	v_exp_f32_e32 v85, v85
	v_cvt_pkrtz_f16_f32 v50, v50, v51
	v_and_b32_e32 v78, v147, v50
	v_cvt_pkrtz_f16_f32 v50, v52, v53
	v_cvt_pkrtz_f16_f32 v82, v82, v83
	v_cvt_pkrtz_f16_f32 v83, v84, v85
	v_exp_f32_e32 v84, v86
	v_exp_f32_e32 v85, v87
	v_and_b32_e32 v79, v148, v50
	v_exp_f32_e32 v86, v88
	v_exp_f32_e32 v87, v89
	v_exp_f32_e32 v50, v62
	v_exp_f32_e32 v51, v63
	v_exp_f32_e32 v52, v64
	v_exp_f32_e32 v53, v65
	v_cvt_pkrtz_f16_f32 v84, v84, v85
	v_cvt_pkrtz_f16_f32 v85, v86, v87
	v_cvt_pkrtz_f16_f32 v50, v50, v51
	v_exp_f32_e32 v86, v90
	v_exp_f32_e32 v87, v91
	v_exp_f32_e32 v88, v92
	v_exp_f32_e32 v89, v93
	v_and_b32_e32 v80, v149, v50
	v_cvt_pkrtz_f16_f32 v50, v52, v53
	v_and_b32_e32 v81, v150, v50
	ds_read_b128 v[50:53], v183
	v_cvt_pkrtz_f16_f32 v86, v86, v87
	v_cvt_pkrtz_f16_f32 v87, v88, v89
	v_exp_f32_e32 v88, v94
	v_exp_f32_e32 v89, v95
	v_exp_f32_e32 v90, v96
	v_exp_f32_e32 v91, v97
	v_exp_f32_e32 v34, v34
	v_exp_f32_e32 v35, v35
	v_exp_f32_e32 v36, v36
	v_exp_f32_e32 v37, v37
	v_and_b32_e32 v82, v127, v82
	v_and_b32_e32 v83, v128, v83
	v_and_b32_e32 v84, v129, v84
	v_and_b32_e32 v85, v130, v85
	v_cvt_pkrtz_f16_f32 v88, v88, v89
	v_cvt_pkrtz_f16_f32 v89, v90, v91
	ds_read_b128 v[90:93], v183 offset:32
	s_waitcnt lgkmcnt(0)
	v_mfma_f32_32x32x16_f16 v[50:65], v[50:53], v[82:85], 0
	v_cvt_pkrtz_f16_f32 v34, v34, v35
	v_cvt_pkrtz_f16_f32 v35, v36, v37
	v_exp_f32_e32 v36, v38
	v_exp_f32_e32 v37, v39
	v_exp_f32_e32 v38, v40
	v_exp_f32_e32 v39, v41
	v_and_b32_e32 v86, v131, v86
	v_and_b32_e32 v87, v132, v87
	v_and_b32_e32 v88, v133, v88
	v_and_b32_e32 v89, v134, v89
	v_cvt_pkrtz_f16_f32 v36, v36, v37
	v_cvt_pkrtz_f16_f32 v37, v38, v39
	ds_read_b128 v[38:41], v183 offset:64
	v_mfma_f32_32x32x16_f16 v[50:65], v[90:93], v[86:89], v[50:65]
	v_mov_b32_e32 v115, 0
	v_dot2c_f32_f16_e32 v115, 0x3c003c00, v82
	v_dot2c_f32_f16_e32 v115, 0x3c003c00, v83
	v_dot2c_f32_f16_e32 v115, 0x3c003c00, v84
	v_dot2c_f32_f16_e32 v115, 0x3c003c00, v85
	v_and_b32_e32 v66, v135, v66
	v_and_b32_e32 v67, v136, v67
	v_and_b32_e32 v68, v137, v68
	v_and_b32_e32 v69, v138, v69
	ds_read_b128 v[82:85], v183 offset:96
	s_waitcnt lgkmcnt(0)
	v_mfma_f32_32x32x16_f16 v[50:65], v[38:41], v[66:69], v[50:65]
	v_exp_f32_e32 v42, v42
	v_exp_f32_e32 v43, v43
	v_and_b32_e32 v70, v139, v70
	v_and_b32_e32 v71, v140, v71
	v_and_b32_e32 v72, v141, v72
	v_and_b32_e32 v73, v142, v73
	v_cvt_pkrtz_f16_f32 v38, v42, v43
	v_exp_f32_e32 v39, v44
	v_exp_f32_e32 v44, v45
	ds_read_b128 v[40:43], v183 offset:128
	v_dot2c_f32_f16_e32 v115, 0x3c003c00, v86
	v_mfma_f32_32x32x16_f16 v[50:65], v[82:85], v[70:73], v[50:65]
	v_dot2c_f32_f16_e32 v115, 0x3c003c00, v87
	v_dot2c_f32_f16_e32 v115, 0x3c003c00, v88
	v_dot2c_f32_f16_e32 v115, 0x3c003c00, v89
	v_dot2c_f32_f16_e32 v115, 0x3c003c00, v66
	v_dot2c_f32_f16_e32 v115, 0x3c003c00, v67
	v_dot2c_f32_f16_e32 v115, 0x3c003c00, v68
	v_dot2c_f32_f16_e32 v115, 0x3c003c00, v69
	ds_read_b128 v[66:69], v183 offset:160
	s_waitcnt lgkmcnt(0)
	v_mfma_f32_32x32x16_f16 v[50:65], v[40:43], v[74:77], v[50:65]
	v_dot2c_f32_f16_e32 v115, 0x3c003c00, v70
	v_dot2c_f32_f16_e32 v115, 0x3c003c00, v71
	v_dot2c_f32_f16_e32 v115, 0x3c003c00, v72
	v_cvt_pkrtz_f16_f32 v39, v39, v44
	v_dot2c_f32_f16_e32 v115, 0x3c003c00, v73
	v_exp_f32_e32 v46, v46
	v_exp_f32_e32 v40, v47
	v_exp_f32_e32 v47, v49
	ds_read_b128 v[42:45], v183 offset:192
	v_dot2c_f32_f16_e32 v115, 0x3c003c00, v74
	v_mfma_f32_32x32x16_f16 v[50:65], v[66:69], v[78:81], v[50:65]
	v_dot2c_f32_f16_e32 v115, 0x3c003c00, v75
	v_dot2c_f32_f16_e32 v115, 0x3c003c00, v76
	v_dot2c_f32_f16_e32 v115, 0x3c003c00, v77
	v_exp_f32_e32 v41, v48
	v_dot2c_f32_f16_e32 v115, 0x3c003c00, v78
	v_dot2c_f32_f16_e32 v115, 0x3c003c00, v79
	v_dot2c_f32_f16_e32 v115, 0x3c003c00, v80
	v_dot2c_f32_f16_e32 v115, 0x3c003c00, v81
	v_and_b32_e32 v34, v151, v34
	v_and_b32_e32 v35, v152, v35
	v_and_b32_e32 v36, v153, v36
	v_and_b32_e32 v37, v154, v37
	v_cvt_pkrtz_f16_f32 v40, v46, v40
	v_cvt_pkrtz_f16_f32 v41, v41, v47
	ds_read_b128 v[46:49], v183 offset:224
	v_dot2c_f32_f16_e32 v115, 0x3c003c00, v34
	s_waitcnt lgkmcnt(0)
	v_mfma_f32_32x32x16_f16 v[50:65], v[42:45], v[34:37], v[50:65]
	v_dot2c_f32_f16_e32 v115, 0x3c003c00, v35
	v_dot2c_f32_f16_e32 v115, 0x3c003c00, v36
	v_dot2c_f32_f16_e32 v115, 0x3c003c00, v37
	v_and_b32_e32 v38, v155, v38
	v_dot2c_f32_f16_e32 v115, 0x3c003c00, v38
	v_and_b32_e32 v39, v156, v39
	v_dot2c_f32_f16_e32 v115, 0x3c003c00, v39
	v_and_b32_e32 v40, v157, v40
	v_dot2c_f32_f16_e32 v115, 0x3c003c00, v40
	v_and_b32_e32 v41, v158, v41
	v_dot2c_f32_f16_e32 v115, 0x3c003c00, v41
	s_nop 0
	v_mfma_f32_32x32x16_f16 v[50:65], v[46:49], v[38:41], v[50:65]
	s_nop 0
	v_mov_b32_e32 v34, v115
	v_mov_b32_e32 v35, v115
	s_nop 1
	v_permlane32_swap_b32_e32 v34, v35
	v_cndmask_b32_e64 v34, v34, v35, s[2:3]
	v_add_f32_e32 v34, v115, v34
	v_rcp_f32_e32 v34, v34
	s_nop 2
	v_mul_f32_e32 v52, v34, v58
	v_mul_f32_e32 v53, v34, v59
	v_mul_f32_e32 v54, v34, v60
	v_mul_f32_e32 v55, v34, v61
	v_mul_f32_e32 v56, v34, v62
	v_mul_f32_e32 v57, v34, v63
	v_mul_f32_e32 v58, v34, v64
	v_mul_f32_e32 v59, v34, v65
	v_cvt_pkrtz_f16_f32 v34, v185, v186
	v_cvt_pkrtz_f16_f32 v35, v187, v188
	v_cvt_pkrtz_f16_f32 v36, v189, v190
	v_cvt_pkrtz_f16_f32 v37, v191, v192
	s_and_b64 vcc, exec, s[20:21]
	s_mov_b64 s[20:21], 0
	s_mov_b32 s18, 1
	v_mov_b32_e32 v114, v179
	v_mov_b32_e32 v115, v180
	v_mov_b32_e32 v116, v181
	v_mov_b32_e32 v117, v182
	s_waitcnt vmcnt(0)
	v_mfma_f32_32x32x16_f16 v[2:17], v[240:243], v[34:37], v[2:17]
	v_cvt_pkrtz_f16_f32 v42, v52, v53
	v_cvt_pkrtz_f16_f32 v43, v54, v55
	v_cvt_pkrtz_f16_f32 v44, v56, v57
	v_cvt_pkrtz_f16_f32 v45, v58, v59
	v_mfma_f32_32x32x16_f16 v[18:33], v[236:239], v[34:37], v[18:33]
	v_mov_b32_e32 v34, v175
	v_mov_b32_e32 v35, v176
	v_mov_b32_e32 v36, v177
	v_mov_b32_e32 v37, v178
	v_mfma_f32_32x32x16_f16 v[18:33], v[244:247], v[42:45], v[18:33]
	v_mfma_f32_32x32x16_f16 v[2:17], v[248:251], v[42:45], v[2:17]
	s_cbranch_vccnz .LBB2_83
	v_cvt_f32_f16_sdwa v67, v110 dst_sel:DWORD dst_unused:UNUSED_PAD src0_sel:WORD_1
	v_cvt_f32_f16_e32 v66, v110
	v_cvt_f32_f16_sdwa v69, v111 dst_sel:DWORD dst_unused:UNUSED_PAD src0_sel:WORD_1
	v_cvt_f32_f16_e32 v68, v111
	v_cvt_f32_f16_sdwa v71, v112 dst_sel:DWORD dst_unused:UNUSED_PAD src0_sel:WORD_1
	v_cvt_f32_f16_e32 v70, v112
	v_cvt_f32_f16_sdwa v73, v113 dst_sel:DWORD dst_unused:UNUSED_PAD src0_sel:WORD_1
	v_cvt_f32_f16_e32 v72, v113
	ds_read_b128 v[34:37], v173 offset:7040
	ds_read_b128 v[38:41], v173 offset:7328
	ds_read_b128 v[42:45], v173 offset:7616
	ds_read_b128 v[46:49], v173 offset:7904
	ds_read_b128 v[50:53], v173 offset:8192
	ds_read_b128 v[54:57], v173 offset:8480
	ds_read_b128 v[58:61], v173 offset:8768
	ds_read_b128 v[62:65], v173 offset:9056
	s_waitcnt lgkmcnt(7)
	v_pk_add_f32 v[18:19], v[34:35], v[18:19]
	v_cvt_f32_f16_sdwa v75, v106 dst_sel:DWORD dst_unused:UNUSED_PAD src0_sel:WORD_1
	v_cvt_f32_f16_e32 v74, v106
	v_cvt_f32_f16_sdwa v83, v102 dst_sel:DWORD dst_unused:UNUSED_PAD src0_sel:WORD_1
	v_cvt_f32_f16_e32 v82, v102
	v_pk_add_f32 v[66:67], v[18:19], v[66:67]
	v_pk_add_f32 v[18:19], v[36:37], v[20:21]
	v_cvt_f32_f16_sdwa v77, v107 dst_sel:DWORD dst_unused:UNUSED_PAD src0_sel:WORD_1
	v_cvt_f32_f16_e32 v76, v107
	v_cvt_f32_f16_sdwa v85, v103 dst_sel:DWORD dst_unused:UNUSED_PAD src0_sel:WORD_1
	v_cvt_f32_f16_e32 v84, v103
	v_pk_add_f32 v[68:69], v[18:19], v[68:69]
	s_waitcnt lgkmcnt(6)
	v_pk_add_f32 v[18:19], v[22:23], v[38:39]
	v_cvt_f32_f16_sdwa v79, v108 dst_sel:DWORD dst_unused:UNUSED_PAD src0_sel:WORD_1
	v_cvt_f32_f16_e32 v78, v108
	v_cvt_f32_f16_sdwa v87, v104 dst_sel:DWORD dst_unused:UNUSED_PAD src0_sel:WORD_1
	v_cvt_f32_f16_e32 v86, v104
	v_pk_add_f32 v[70:71], v[18:19], v[70:71]
	v_pk_add_f32 v[18:19], v[24:25], v[40:41]
	v_cvt_f32_f16_sdwa v89, v105 dst_sel:DWORD dst_unused:UNUSED_PAD src0_sel:WORD_1
	v_cvt_f32_f16_e32 v88, v105
	v_pk_add_f32 v[72:73], v[18:19], v[72:73]
	s_waitcnt lgkmcnt(5)
	v_pk_add_f32 v[18:19], v[26:27], v[42:43]
	s_waitcnt lgkmcnt(3)
	v_pk_add_f32 v[2:3], v[50:51], v[2:3]
	v_cvt_f32_f16_sdwa v91, v98 dst_sel:DWORD dst_unused:UNUSED_PAD src0_sel:WORD_1
	v_cvt_f32_f16_e32 v90, v98
	v_pk_add_f32 v[74:75], v[18:19], v[74:75]
	v_pk_add_f32 v[18:19], v[28:29], v[44:45]
	v_pk_add_f32 v[44:45], v[2:3], v[82:83]
	v_pk_add_f32 v[2:3], v[52:53], v[4:5]
	v_cvt_f32_f16_sdwa v93, v99 dst_sel:DWORD dst_unused:UNUSED_PAD src0_sel:WORD_1
	v_cvt_f32_f16_e32 v92, v99
	v_pk_add_f32 v[76:77], v[18:19], v[76:77]
	v_pk_add_f32 v[18:19], v[30:31], v[46:47]
	v_pk_add_f32 v[46:47], v[2:3], v[84:85]
	s_waitcnt lgkmcnt(2)
	v_pk_add_f32 v[2:3], v[6:7], v[54:55]
	v_cvt_f32_f16_sdwa v95, v100 dst_sel:DWORD dst_unused:UNUSED_PAD src0_sel:WORD_1
	v_cvt_f32_f16_e32 v94, v100
	v_pk_add_f32 v[78:79], v[18:19], v[78:79]
	v_pk_add_f32 v[18:19], v[32:33], v[48:49]
	v_pk_add_f32 v[48:49], v[2:3], v[86:87]
	v_pk_add_f32 v[2:3], v[8:9], v[56:57]
	v_cvt_f32_f16_sdwa v97, v101 dst_sel:DWORD dst_unused:UNUSED_PAD src0_sel:WORD_1
	v_cvt_f32_f16_e32 v96, v101
	v_pk_add_f32 v[50:51], v[2:3], v[88:89]
	s_waitcnt lgkmcnt(1)
	v_pk_add_f32 v[2:3], v[10:11], v[58:59]
	v_cvt_f32_f16_sdwa v81, v109 dst_sel:DWORD dst_unused:UNUSED_PAD src0_sel:WORD_1
	v_pk_add_f32 v[52:53], v[2:3], v[90:91]
	v_pk_add_f32 v[2:3], v[12:13], v[60:61]
	v_cvt_f32_f16_e32 v80, v109
	v_pk_add_f32 v[54:55], v[2:3], v[92:93]
	s_waitcnt lgkmcnt(0)
	v_pk_add_f32 v[2:3], v[14:15], v[62:63]
	s_add_i32 s15, 0, 0x16000
	v_pk_add_f32 v[56:57], v[2:3], v[94:95]
	v_pk_add_f32 v[2:3], v[16:17], v[64:65]
	v_pk_add_f32 v[80:81], v[18:19], v[80:81]
	v_pk_add_f32 v[58:59], v[2:3], v[96:97]
	v_add_f32_e32 v3, 0, v66
	v_add_f32_e32 v3, v67, v3
	v_add_f32_e32 v3, v68, v3
	v_add_f32_e32 v3, v69, v3
	v_add_f32_e32 v3, v70, v3
	v_add_f32_e32 v3, v71, v3
	v_add_f32_e32 v3, v72, v3
	v_add_f32_e32 v3, v73, v3
	v_add_f32_e32 v3, v74, v3
	v_add_f32_e32 v3, v75, v3
	v_add_f32_e32 v3, v76, v3
	v_add_f32_e32 v3, v77, v3
	v_add_f32_e32 v3, v78, v3
	v_add_f32_e32 v3, v79, v3
	v_add_f32_e32 v3, v80, v3
	v_add_f32_e32 v3, v81, v3
	v_add_f32_e32 v3, v44, v3
	v_add_f32_e32 v3, v45, v3
	v_add_f32_e32 v3, v46, v3
	v_add_f32_e32 v3, v47, v3
	v_add_f32_e32 v3, v48, v3
	v_add_f32_e32 v3, v49, v3
	v_add_f32_e32 v3, v50, v3
	v_add_f32_e32 v3, v51, v3
	v_add_f32_e32 v3, v52, v3
	v_add_f32_e32 v3, v53, v3
	v_add_f32_e32 v3, v54, v3
	v_add_f32_e32 v3, v55, v3
	v_add_f32_e32 v3, v56, v3
	v_add_f32_e32 v3, v57, v3
	v_add_f32_e32 v3, v58, v3
	v_add_f32_e32 v3, v59, v3
	v_mov_b32_e32 v4, v3
	v_mov_b32_e32 v5, v3
	s_nop 1
	v_permlane32_swap_b32_e32 v4, v5
	v_cndmask_b32_e64 v4, v4, v5, s[2:3]
	v_add_f32_e32 v3, v3, v4
	v_mul_f32_e32 v60, 0x3c800000, v3
	v_or_b32_e32 v3, 0x100, v126
	v_lshrrev_b32_e32 v3, 2, v3
	s_movk_i32 s18, 0x90
	v_mov_b32_e32 v4, s15
	v_pk_add_f32 v[66:67], v[66:67], v[60:61] op_sel_hi:[1,0] neg_lo:[0,1] neg_hi:[0,1]
	v_mad_u32_u24 v3, v3, s18, v4
	v_pk_mul_f32 v[114:115], v[66:67], v[66:67]
	v_pk_add_f32 v[116:117], v[68:69], v[60:61] op_sel_hi:[1,0] neg_lo:[0,1] neg_hi:[0,1]
	ds_read_b128 v[4:7], v3 offset:128
	ds_read_b128 v[8:11], v173 offset:11648
	ds_read_b128 v[12:15], v173 offset:9632
	ds_read_b128 v[16:19], v173 offset:9920
	ds_read_b128 v[20:23], v173 offset:11936
	ds_read_b128 v[24:27], v173 offset:12224
	ds_read_b128 v[28:31], v173 offset:10208
	ds_read_b128 v[32:35], v173 offset:10496
	ds_read_b128 v[36:39], v173 offset:12512
	ds_read_b128 v[40:43], v173 offset:12800
	v_pk_add_f32 v[64:65], v[44:45], v[60:61] op_sel_hi:[1,0] neg_lo:[0,1] neg_hi:[0,1]
	v_pk_add_f32 v[86:87], v[46:47], v[60:61] op_sel_hi:[1,0] neg_lo:[0,1] neg_hi:[0,1]
	v_pk_add_f32 v[88:89], v[48:49], v[60:61] op_sel_hi:[1,0] neg_lo:[0,1] neg_hi:[0,1]
	v_pk_add_f32 v[90:91], v[50:51], v[60:61] op_sel_hi:[1,0] neg_lo:[0,1] neg_hi:[0,1]
	v_pk_add_f32 v[98:99], v[52:53], v[60:61] op_sel_hi:[1,0] neg_lo:[0,1] neg_hi:[0,1]
	v_pk_add_f32 v[100:101], v[54:55], v[60:61] op_sel_hi:[1,0] neg_lo:[0,1] neg_hi:[0,1]
	v_pk_add_f32 v[102:103], v[56:57], v[60:61] op_sel_hi:[1,0] neg_lo:[0,1] neg_hi:[0,1]
	v_pk_add_f32 v[104:105], v[58:59], v[60:61] op_sel_hi:[1,0] neg_lo:[0,1] neg_hi:[0,1]
	v_pk_add_f32 v[78:79], v[78:79], v[60:61] op_sel_hi:[1,0] neg_lo:[0,1] neg_hi:[0,1]
	v_pk_add_f32 v[80:81], v[80:81], v[60:61] op_sel_hi:[1,0] neg_lo:[0,1] neg_hi:[0,1]
	v_pk_add_f32 v[74:75], v[74:75], v[60:61] op_sel_hi:[1,0] neg_lo:[0,1] neg_hi:[0,1]
	v_pk_add_f32 v[76:77], v[76:77], v[60:61] op_sel_hi:[1,0] neg_lo:[0,1] neg_hi:[0,1]
	v_pk_add_f32 v[70:71], v[70:71], v[60:61] op_sel_hi:[1,0] neg_lo:[0,1] neg_hi:[0,1]
	v_pk_add_f32 v[72:73], v[72:73], v[60:61] op_sel_hi:[1,0] neg_lo:[0,1] neg_hi:[0,1]
	v_pk_mul_f32 v[60:61], v[116:117], v[116:117]
	v_add_f32_e32 v3, v114, v115
	v_add_f32_e32 v3, v60, v3
	v_pk_mul_f32 v[110:111], v[70:71], v[70:71]
	v_add_f32_e32 v3, v61, v3
	v_add_f32_e32 v3, v110, v3
	v_pk_mul_f32 v[112:113], v[72:73], v[72:73]
	v_add_f32_e32 v3, v111, v3
	v_add_f32_e32 v3, v112, v3
	v_pk_mul_f32 v[106:107], v[74:75], v[74:75]
	v_add_f32_e32 v3, v113, v3
	v_add_f32_e32 v3, v106, v3
	v_pk_mul_f32 v[108:109], v[76:77], v[76:77]
	v_add_f32_e32 v3, v107, v3
	v_add_f32_e32 v3, v108, v3
	v_pk_mul_f32 v[94:95], v[78:79], v[78:79]
	v_add_f32_e32 v3, v109, v3
	v_add_f32_e32 v3, v94, v3
	v_pk_mul_f32 v[96:97], v[80:81], v[80:81]
	v_add_f32_e32 v3, v95, v3
	v_add_f32_e32 v3, v96, v3
	v_pk_mul_f32 v[62:63], v[64:65], v[64:65]
	v_add_f32_e32 v3, v97, v3
	v_add_f32_e32 v3, v62, v3
	v_pk_mul_f32 v[82:83], v[86:87], v[86:87]
	v_add_f32_e32 v3, v63, v3
	v_add_f32_e32 v3, v82, v3
	v_pk_mul_f32 v[84:85], v[88:89], v[88:89]
	v_add_f32_e32 v3, v83, v3
	v_add_f32_e32 v3, v84, v3
	v_pk_mul_f32 v[92:93], v[90:91], v[90:91]
	v_add_f32_e32 v3, v85, v3
	v_add_f32_e32 v3, v92, v3
	v_pk_mul_f32 v[52:53], v[98:99], v[98:99]
	v_add_f32_e32 v3, v93, v3
	v_add_f32_e32 v3, v52, v3
	v_pk_mul_f32 v[54:55], v[100:101], v[100:101]
	v_add_f32_e32 v3, v53, v3
	v_add_f32_e32 v3, v54, v3
	v_pk_mul_f32 v[56:57], v[102:103], v[102:103]
	v_add_f32_e32 v3, v55, v3
	v_add_f32_e32 v3, v56, v3
	v_pk_mul_f32 v[58:59], v[104:105], v[104:105]
	v_add_f32_e32 v3, v57, v3
	v_add_f32_e32 v3, v58, v3
	v_add_f32_e32 v3, v59, v3
	v_mov_b32_e32 v52, v3
	v_mov_b32_e32 v53, v3
	s_nop 1
	v_permlane32_swap_b32_e32 v52, v53
	v_cndmask_b32_e64 v52, v52, v53, s[2:3]
	v_add_f32_e32 v3, v3, v52
	v_mov_b32_e32 v52, 0x3727c5ac
	v_fmac_f32_e32 v52, 0x3c800000, v3
	v_rsq_f32_e32 v106, v52
	ds_read_b128 v[44:47], v173 offset:10784
	ds_read_b128 v[48:51], v173 offset:11072
	ds_read_b128 v[52:55], v173 offset:13088
	ds_read_b128 v[56:59], v173 offset:13376
	ds_read_b128 v[60:63], v173 offset:11360
	ds_read_b128 v[82:85], v173 offset:13664
	v_mov_b32_e32 v2, 0
	v_pk_mul_f32 v[66:67], v[66:67], v[106:107] op_sel_hi:[1,0]
	s_mov_b32 s15, 8
	s_waitcnt lgkmcnt(14)
	v_pk_fma_f32 v[68:69], v[4:5], v[66:67], v[8:9]
	v_pk_mul_f32 v[4:5], v[116:117], v[106:107] op_sel_hi:[1,0]
	v_mov_b32_e32 v3, v2
	v_pk_fma_f32 v[66:67], v[6:7], v[4:5], v[10:11]
	v_pk_mul_f32 v[4:5], v[70:71], v[106:107] op_sel_hi:[1,0]
	v_mov_b32_e32 v6, v2
	s_waitcnt lgkmcnt(11)
	v_pk_fma_f32 v[70:71], v[12:13], v[4:5], v[20:21]
	v_pk_mul_f32 v[4:5], v[72:73], v[106:107] op_sel_hi:[1,0]
	v_mov_b32_e32 v7, v2
	v_pk_fma_f32 v[72:73], v[14:15], v[4:5], v[22:23]
	v_pk_mul_f32 v[4:5], v[74:75], v[106:107] op_sel_hi:[1,0]
	v_mov_b32_e32 v8, v2
	s_waitcnt lgkmcnt(10)
	v_pk_fma_f32 v[74:75], v[16:17], v[4:5], v[24:25]
	v_pk_mul_f32 v[4:5], v[76:77], v[106:107] op_sel_hi:[1,0]
	v_mov_b32_e32 v9, v2
	v_pk_fma_f32 v[76:77], v[18:19], v[4:5], v[26:27]
	v_pk_mul_f32 v[4:5], v[78:79], v[106:107] op_sel_hi:[1,0]
	v_mov_b32_e32 v10, v2
	s_waitcnt lgkmcnt(7)
	v_pk_fma_f32 v[78:79], v[28:29], v[4:5], v[36:37]
	v_pk_mul_f32 v[4:5], v[80:81], v[106:107] op_sel_hi:[1,0]
	v_mov_b32_e32 v11, v2
	v_pk_fma_f32 v[80:81], v[30:31], v[4:5], v[38:39]
	v_pk_mul_f32 v[4:5], v[64:65], v[106:107] op_sel_hi:[1,0]
	v_mov_b32_e32 v12, v2
	s_waitcnt lgkmcnt(6)
	v_pk_fma_f32 v[96:97], v[32:33], v[4:5], v[40:41]
	v_pk_mul_f32 v[4:5], v[86:87], v[106:107] op_sel_hi:[1,0]
	v_mov_b32_e32 v13, v2
	v_pk_fma_f32 v[94:95], v[34:35], v[4:5], v[42:43]
	v_pk_mul_f32 v[4:5], v[88:89], v[106:107] op_sel_hi:[1,0]
	v_mov_b32_e32 v14, v2
	s_waitcnt lgkmcnt(3)
	v_pk_fma_f32 v[92:93], v[44:45], v[4:5], v[52:53]
	v_pk_mul_f32 v[4:5], v[90:91], v[106:107] op_sel_hi:[1,0]
	v_cvt_pkrtz_f16_f32 v52, v70, v71
	v_pk_fma_f32 v[90:91], v[46:47], v[4:5], v[54:55]
	v_pk_mul_f32 v[4:5], v[98:99], v[106:107] op_sel_hi:[1,0]
	v_cvt_pkrtz_f16_f32 v53, v72, v73
	s_waitcnt lgkmcnt(2)
	v_pk_fma_f32 v[88:89], v[48:49], v[4:5], v[56:57]
	v_pk_mul_f32 v[4:5], v[100:101], v[106:107] op_sel_hi:[1,0]
	v_cvt_pkrtz_f16_f32 v54, v74, v75
	v_pk_fma_f32 v[86:87], v[50:51], v[4:5], v[58:59]
	v_pk_mul_f32 v[4:5], v[102:103], v[106:107] op_sel_hi:[1,0]
	v_cvt_pkrtz_f16_f32 v50, v68, v69
	s_waitcnt lgkmcnt(0)
	v_pk_fma_f32 v[82:83], v[60:61], v[4:5], v[82:83]
	v_pk_mul_f32 v[4:5], v[104:105], v[106:107] op_sel_hi:[1,0]
	v_cvt_pkrtz_f16_f32 v51, v66, v67
	v_pk_fma_f32 v[84:85], v[62:63], v[4:5], v[84:85]
	v_cvt_pkrtz_f16_f32 v55, v76, v77
	v_cvt_pkrtz_f16_f32 v56, v78, v79
	v_cvt_pkrtz_f16_f32 v57, v80, v81
	v_cvt_pkrtz_f16_f32 v58, v96, v97
	v_cvt_pkrtz_f16_f32 v59, v94, v95
	v_cvt_pkrtz_f16_f32 v60, v92, v93
	v_cvt_pkrtz_f16_f32 v61, v90, v91
	v_cvt_pkrtz_f16_f32 v62, v88, v89
	v_cvt_pkrtz_f16_f32 v63, v86, v87
	v_cvt_pkrtz_f16_f32 v64, v82, v83
	v_cvt_pkrtz_f16_f32 v65, v84, v85
	v_mul_u32_u24_e32 v98, 0x90, v164
	v_or_b32_e32 v99, 0x6000, v170
	v_mov_b32_e32 v4, v2
	v_mov_b32_e32 v5, v2
	v_mov_b32_e32 v15, v2
	v_mov_b32_e32 v16, v2
	v_mov_b32_e32 v17, v2
	v_mov_b32_e32 v18, v2
	v_mov_b32_e32 v19, v2
	v_mov_b32_e32 v20, v2
	v_mov_b32_e32 v21, v2
	v_mov_b32_e32 v22, v2
	v_mov_b32_e32 v23, v2
	v_mov_b32_e32 v24, v2
	v_mov_b32_e32 v25, v2
	v_mov_b32_e32 v26, v2
	v_mov_b32_e32 v27, v2
	v_mov_b32_e32 v28, v2
	v_mov_b32_e32 v29, v2
	v_mov_b32_e32 v30, v2
	v_mov_b32_e32 v31, v2
	v_mov_b32_e32 v32, v2
	v_mov_b32_e32 v33, v2
	v_mov_b32_e32 v194, v99
	v_add_u32_e32 v195, 0x1a880, v98
	v_mov_b32_e32 v236, v170
	v_add_u32_e32 v237, 0x12000, v170
	s_mov_b32 s15, 8
.Lmy_ffn3_k2:
	ds_read_b128 v[34:37], v195
	ds_read_b128 v[38:41], v195 offset:288
	ds_read_b128 v[42:45], v195 offset:576
	ds_read_b128 v[46:49], v195 offset:864
	ds_read_b128 v[196:199], v194
	ds_read_b128 v[200:203], v194 offset:1024
	ds_read_b128 v[204:207], v194 offset:2048
	ds_read_b128 v[208:211], v194 offset:3072
	v_add_u32_e32 v194, 0x1000, v194
	v_add_u32_e32 v195, 0x480, v195
	s_add_i32 s15, s15, -1
	s_waitcnt lgkmcnt(3)
	v_mfma_f32_32x32x16_f16 v[34:49], v[196:199], v[50:53], v[34:49]
	s_waitcnt lgkmcnt(2)
	v_mfma_f32_32x32x16_f16 v[34:49], v[200:203], v[54:57], v[34:49]
	s_waitcnt lgkmcnt(1)
	v_mfma_f32_32x32x16_f16 v[34:49], v[204:207], v[58:61], v[34:49]
	s_waitcnt lgkmcnt(0)
	v_mfma_f32_32x32x16_f16 v[34:49], v[208:211], v[62:65], v[34:49]
	ds_read_b128 v[100:103], v236 offset:57344
	ds_read_b128 v[186:189], v237
	ds_read_b128 v[112:115], v236 offset:58368
	ds_read_b128 v[190:193], v237 offset:1024
	v_add_u32_e32 v236, 0x800, v236
	v_add_u32_e32 v237, 0x800, v237
	s_cmp_lg_u32 s15, 0
	s_nop 4
	v_max_f32_e32 v34, 0, v34
	v_max_f32_e32 v35, 0, v35
	v_max_f32_e32 v36, 0, v36
	v_max_f32_e32 v37, 0, v37
	v_max_f32_e32 v38, 0, v38
	v_max_f32_e32 v39, 0, v39
	v_max_f32_e32 v40, 0, v40
	v_max_f32_e32 v41, 0, v41
	v_cvt_pkrtz_f16_f32 v34, v34, v35
	v_cvt_pkrtz_f16_f32 v35, v36, v37
	v_cvt_pkrtz_f16_f32 v36, v38, v39
	v_cvt_pkrtz_f16_f32 v37, v40, v41
	s_waitcnt lgkmcnt(2)
	s_nop 0
	v_mfma_f32_32x32x16_f16 v[18:33], v[100:103], v[34:37], v[18:33]
	v_mfma_f32_32x32x16_f16 v[2:17], v[186:189], v[34:37], v[2:17]
	v_max_f32_e32 v42, 0, v42
	v_max_f32_e32 v43, 0, v43
	v_max_f32_e32 v44, 0, v44
	v_max_f32_e32 v45, 0, v45
	v_max_f32_e32 v46, 0, v46
	v_max_f32_e32 v47, 0, v47
	v_max_f32_e32 v48, 0, v48
	v_max_f32_e32 v49, 0, v49
	v_cvt_pkrtz_f16_f32 v34, v42, v43
	v_cvt_pkrtz_f16_f32 v35, v44, v45
	v_cvt_pkrtz_f16_f32 v36, v46, v47
	v_cvt_pkrtz_f16_f32 v37, v48, v49
	s_waitcnt lgkmcnt(0)
	s_nop 0
	v_mfma_f32_32x32x16_f16 v[18:33], v[112:115], v[34:37], v[18:33]
	v_mfma_f32_32x32x16_f16 v[2:17], v[190:193], v[34:37], v[2:17]
	s_cbranch_scc1 .Lmy_ffn3_k2
	ds_read_b128 v[34:37], v173 offset:27776
	ds_read_b128 v[38:41], v173 offset:28064
	ds_read_b128 v[42:45], v173 offset:28352
	ds_read_b128 v[46:49], v173 offset:28640
	ds_read_b128 v[50:53], v173 offset:28928
	ds_read_b128 v[54:57], v173 offset:29216
	ds_read_b128 v[58:61], v173 offset:29504
	ds_read_b128 v[62:65], v173 offset:29792
	ds_read_b128 v[98:101], v173 offset:13952
	ds_read_b128 v[102:105], v173 offset:14240
	ds_read_b128 v[106:109], v173 offset:16256
	ds_read_b128 v[110:113], v173 offset:16544
	ds_read_b128 v[114:117], v173 offset:14528
	ds_read_b128 v[174:177], v173 offset:14816
	ds_read_b128 v[178:181], v173 offset:16832
	ds_read_b128 v[182:185], v173 offset:17120
	s_waitcnt lgkmcnt(14)
	v_pk_add_f32 v[18:19], v[18:19], v[34:35]
	v_pk_add_f32 v[20:21], v[20:21], v[36:37]
	v_pk_add_f32 v[18:19], v[68:69], v[18:19]
	v_pk_add_f32 v[20:21], v[66:67], v[20:21]
	v_add_f32_e32 v34, 0, v18
	v_add_f32_e32 v34, v19, v34
	v_pk_add_f32 v[22:23], v[22:23], v[38:39]
	v_add_f32_e32 v34, v20, v34
	v_pk_add_f32 v[22:23], v[70:71], v[22:23]
	v_add_f32_e32 v34, v21, v34
	v_pk_add_f32 v[24:25], v[24:25], v[40:41]
	v_add_f32_e32 v34, v22, v34
	v_pk_add_f32 v[24:25], v[72:73], v[24:25]
	v_add_f32_e32 v34, v23, v34
	s_waitcnt lgkmcnt(13)
	v_pk_add_f32 v[26:27], v[26:27], v[42:43]
	v_add_f32_e32 v34, v24, v34
	v_pk_add_f32 v[26:27], v[74:75], v[26:27]
	v_add_f32_e32 v34, v25, v34
	v_pk_add_f32 v[28:29], v[28:29], v[44:45]
	v_add_f32_e32 v34, v26, v34
	v_pk_add_f32 v[28:29], v[76:77], v[28:29]
	v_add_f32_e32 v34, v27, v34
	s_waitcnt lgkmcnt(12)
	v_pk_add_f32 v[30:31], v[30:31], v[46:47]
	v_add_f32_e32 v34, v28, v34
	v_pk_add_f32 v[30:31], v[78:79], v[30:31]
	v_add_f32_e32 v34, v29, v34
	v_pk_add_f32 v[32:33], v[32:33], v[48:49]
	v_add_f32_e32 v34, v30, v34
	v_pk_add_f32 v[32:33], v[80:81], v[32:33]
	v_add_f32_e32 v34, v31, v34
	s_waitcnt lgkmcnt(11)
	v_pk_add_f32 v[2:3], v[2:3], v[50:51]
	v_add_f32_e32 v34, v32, v34
	v_pk_add_f32 v[96:97], v[96:97], v[2:3]
	v_add_f32_e32 v34, v33, v34
	v_pk_add_f32 v[2:3], v[4:5], v[52:53]
	v_add_f32_e32 v34, v96, v34
	v_pk_add_f32 v[94:95], v[94:95], v[2:3]
	v_add_f32_e32 v34, v97, v34
	s_waitcnt lgkmcnt(10)
	v_pk_add_f32 v[6:7], v[6:7], v[54:55]
	v_add_f32_e32 v34, v94, v34
	v_pk_add_f32 v[6:7], v[92:93], v[6:7]
	v_add_f32_e32 v34, v95, v34
	v_pk_add_f32 v[8:9], v[8:9], v[56:57]
	v_add_f32_e32 v34, v6, v34
	v_pk_add_f32 v[8:9], v[90:91], v[8:9]
	v_add_f32_e32 v34, v7, v34
	s_waitcnt lgkmcnt(9)
	v_pk_add_f32 v[10:11], v[10:11], v[58:59]
	v_add_f32_e32 v34, v8, v34
	v_pk_add_f32 v[10:11], v[88:89], v[10:11]
	v_add_f32_e32 v34, v9, v34
	v_pk_add_f32 v[12:13], v[12:13], v[60:61]
	v_add_f32_e32 v34, v10, v34
	v_pk_add_f32 v[12:13], v[86:87], v[12:13]
	v_add_f32_e32 v34, v11, v34
	s_waitcnt lgkmcnt(8)
	v_pk_add_f32 v[14:15], v[14:15], v[62:63]
	v_add_f32_e32 v34, v12, v34
	v_pk_add_f32 v[14:15], v[82:83], v[14:15]
	v_add_f32_e32 v34, v13, v34
	v_pk_add_f32 v[16:17], v[16:17], v[64:65]
	v_add_f32_e32 v34, v14, v34
	v_pk_add_f32 v[16:17], v[84:85], v[16:17]
	v_add_f32_e32 v34, v15, v34
	v_add_f32_e32 v34, v16, v34
	v_add_f32_e32 v34, v17, v34
	v_mov_b32_e32 v35, v34
	v_mov_b32_e32 v36, v34
	s_nop 1
	v_permlane32_swap_b32_e32 v35, v36
	v_cndmask_b32_e64 v35, v35, v36, s[2:3]
	v_add_f32_e32 v34, v34, v35
	v_mul_f32_e32 v34, 0x3c800000, v34
	v_pk_add_f32 v[36:37], v[18:19], v[34:35] op_sel_hi:[1,0] neg_lo:[0,1] neg_hi:[0,1]
	v_pk_add_f32 v[38:39], v[20:21], v[34:35] op_sel_hi:[1,0] neg_lo:[0,1] neg_hi:[0,1]
	v_pk_mul_f32 v[18:19], v[36:37], v[36:37]
	v_pk_mul_f32 v[20:21], v[38:39], v[38:39]
	v_add_f32_e32 v18, v18, v19
	v_pk_add_f32 v[22:23], v[22:23], v[34:35] op_sel_hi:[1,0] neg_lo:[0,1] neg_hi:[0,1]
	v_add_f32_e32 v18, v20, v18
	v_pk_mul_f32 v[40:41], v[22:23], v[22:23]
	v_add_f32_e32 v18, v21, v18
	v_pk_add_f32 v[24:25], v[24:25], v[34:35] op_sel_hi:[1,0] neg_lo:[0,1] neg_hi:[0,1]
	v_add_f32_e32 v18, v40, v18
	v_pk_mul_f32 v[42:43], v[24:25], v[24:25]
	v_add_f32_e32 v18, v41, v18
	v_pk_add_f32 v[26:27], v[26:27], v[34:35] op_sel_hi:[1,0] neg_lo:[0,1] neg_hi:[0,1]
	v_add_f32_e32 v18, v42, v18
	v_pk_mul_f32 v[44:45], v[26:27], v[26:27]
	v_add_f32_e32 v18, v43, v18
	v_pk_add_f32 v[28:29], v[28:29], v[34:35] op_sel_hi:[1,0] neg_lo:[0,1] neg_hi:[0,1]
	v_add_f32_e32 v18, v44, v18
	v_pk_mul_f32 v[46:47], v[28:29], v[28:29]
	v_add_f32_e32 v18, v45, v18
	v_pk_add_f32 v[30:31], v[30:31], v[34:35] op_sel_hi:[1,0] neg_lo:[0,1] neg_hi:[0,1]
	v_add_f32_e32 v18, v46, v18
	v_pk_mul_f32 v[48:49], v[30:31], v[30:31]
	v_add_f32_e32 v18, v47, v18
	v_pk_add_f32 v[32:33], v[32:33], v[34:35] op_sel_hi:[1,0] neg_lo:[0,1] neg_hi:[0,1]
	v_add_f32_e32 v18, v48, v18
	v_pk_mul_f32 v[54:55], v[32:33], v[32:33]
	v_add_f32_e32 v18, v49, v18
	v_pk_add_f32 v[56:57], v[96:97], v[34:35] op_sel_hi:[1,0] neg_lo:[0,1] neg_hi:[0,1]
	v_add_f32_e32 v18, v54, v18
	v_pk_mul_f32 v[58:59], v[56:57], v[56:57]
	v_add_f32_e32 v18, v55, v18
	v_pk_add_f32 v[60:61], v[94:95], v[34:35] op_sel_hi:[1,0] neg_lo:[0,1] neg_hi:[0,1]
	v_add_f32_e32 v18, v58, v18
	v_pk_mul_f32 v[62:63], v[60:61], v[60:61]
	v_add_f32_e32 v18, v59, v18
	v_pk_add_f32 v[64:65], v[6:7], v[34:35] op_sel_hi:[1,0] neg_lo:[0,1] neg_hi:[0,1]
	v_add_f32_e32 v18, v62, v18
	v_pk_mul_f32 v[6:7], v[64:65], v[64:65]
	v_add_f32_e32 v18, v63, v18
	v_pk_add_f32 v[66:67], v[8:9], v[34:35] op_sel_hi:[1,0] neg_lo:[0,1] neg_hi:[0,1]
	v_add_f32_e32 v6, v6, v18
	v_pk_mul_f32 v[8:9], v[66:67], v[66:67]
	v_add_f32_e32 v6, v7, v6
	v_pk_add_f32 v[68:69], v[10:11], v[34:35] op_sel_hi:[1,0] neg_lo:[0,1] neg_hi:[0,1]
	v_add_f32_e32 v6, v8, v6
	v_pk_mul_f32 v[10:11], v[68:69], v[68:69]
	v_add_f32_e32 v6, v9, v6
	v_pk_add_f32 v[70:71], v[12:13], v[34:35] op_sel_hi:[1,0] neg_lo:[0,1] neg_hi:[0,1]
	v_add_f32_e32 v6, v10, v6
	v_pk_mul_f32 v[12:13], v[70:71], v[70:71]
	v_add_f32_e32 v6, v11, v6
	v_pk_add_f32 v[72:73], v[14:15], v[34:35] op_sel_hi:[1,0] neg_lo:[0,1] neg_hi:[0,1]
	v_add_f32_e32 v6, v12, v6
	v_pk_mul_f32 v[14:15], v[72:73], v[72:73]
	v_add_f32_e32 v6, v13, v6
	v_pk_add_f32 v[34:35], v[16:17], v[34:35] op_sel_hi:[1,0] neg_lo:[0,1] neg_hi:[0,1]
	v_add_f32_e32 v6, v14, v6
	v_pk_mul_f32 v[16:17], v[34:35], v[34:35]
	v_add_f32_e32 v6, v15, v6
	v_add_f32_e32 v6, v16, v6
	v_add_f32_e32 v6, v17, v6
	v_mov_b32_e32 v7, v6
	v_mov_b32_e32 v8, v6
	s_nop 1
	v_permlane32_swap_b32_e32 v7, v8
	v_cndmask_b32_e64 v7, v7, v8, s[2:3]
	v_add_f32_e32 v6, v6, v7
	v_mov_b32_e32 v7, 0x3727c5ac
	v_fmac_f32_e32 v7, 0x3c800000, v6
	v_rsq_f32_e32 v40, v7
	ds_read_b128 v[2:5], v173 offset:15104
	ds_read_b128 v[50:53], v173 offset:15392
	ds_read_b128 v[186:189], v173 offset:17408
	ds_read_b128 v[190:193], v173 offset:17696
	ds_read_b128 v[6:9], v173 offset:15680
	ds_read_b128 v[10:13], v173 offset:15968
	ds_read_b128 v[14:17], v173 offset:17984
	ds_read_b128 v[18:21], v173 offset:18272
	s_load_dwordx2 s[0:1], s[0:1], 0x80
	v_pk_mul_f32 v[22:23], v[22:23], v[40:41] op_sel_hi:[1,0]
	v_pk_mul_f32 v[36:37], v[36:37], v[40:41] op_sel_hi:[1,0]
	s_waitcnt lgkmcnt(0)
	v_pk_fma_f32 v[82:83], v[102:103], v[22:23], v[110:111]
	v_pk_mul_f32 v[22:23], v[24:25], v[40:41] op_sel_hi:[1,0]
	v_pk_fma_f32 v[74:75], v[98:99], v[36:37], v[106:107]
	v_pk_fma_f32 v[84:85], v[104:105], v[22:23], v[112:113]
	v_pk_mul_f32 v[22:23], v[26:27], v[40:41] op_sel_hi:[1,0]
	v_pk_mul_f32 v[36:37], v[38:39], v[40:41] op_sel_hi:[1,0]
	v_pk_fma_f32 v[86:87], v[114:115], v[22:23], v[178:179]
	v_pk_mul_f32 v[22:23], v[28:29], v[40:41] op_sel_hi:[1,0]
	v_pk_fma_f32 v[76:77], v[100:101], v[36:37], v[108:109]
	v_pk_fma_f32 v[88:89], v[116:117], v[22:23], v[180:181]
	v_pk_mul_f32 v[22:23], v[30:31], v[40:41] op_sel_hi:[1,0]
	s_nop 0
	v_pk_fma_f32 v[94:95], v[174:175], v[22:23], v[182:183]
	v_pk_mul_f32 v[22:23], v[32:33], v[40:41] op_sel_hi:[1,0]
	s_nop 0
	v_pk_fma_f32 v[110:111], v[176:177], v[22:23], v[184:185]
	v_pk_mul_f32 v[22:23], v[56:57], v[40:41] op_sel_hi:[1,0]
	s_nop 0
	v_pk_fma_f32 v[108:109], v[2:3], v[22:23], v[186:187]
	v_pk_mul_f32 v[2:3], v[60:61], v[40:41] op_sel_hi:[1,0]
	s_nop 0
	v_pk_fma_f32 v[106:107], v[4:5], v[2:3], v[188:189]
	v_pk_mul_f32 v[2:3], v[64:65], v[40:41] op_sel_hi:[1,0]
	s_nop 0
	v_pk_fma_f32 v[104:105], v[50:51], v[2:3], v[190:191]
	v_pk_mul_f32 v[2:3], v[66:67], v[40:41] op_sel_hi:[1,0]
	s_nop 0
	v_pk_fma_f32 v[100:101], v[52:53], v[2:3], v[192:193]
	v_pk_mul_f32 v[2:3], v[68:69], v[40:41] op_sel_hi:[1,0]
	s_nop 0
	v_pk_fma_f32 v[96:97], v[6:7], v[2:3], v[14:15]
	v_pk_mul_f32 v[2:3], v[70:71], v[40:41] op_sel_hi:[1,0]
	s_nop 0
	v_pk_fma_f32 v[92:93], v[8:9], v[2:3], v[16:17]
	v_pk_mul_f32 v[2:3], v[72:73], v[40:41] op_sel_hi:[1,0]
	s_nop 0
	v_pk_fma_f32 v[90:91], v[10:11], v[2:3], v[18:19]
	v_pk_mul_f32 v[2:3], v[34:35], v[40:41] op_sel_hi:[1,0]
	s_nop 0
	v_pk_fma_f32 v[102:103], v[12:13], v[2:3], v[20:21]
	v_lshl_add_u64 v[2:3], v[118:119], 1, s[0:1]
	v_lshlrev_b32_e32 v98, 1, v126
	v_mov_b32_e32 v99, 0
	v_lshl_add_u64 v[2:3], v[2:3], 0, v[98:99]
	v_cvt_pk_f16_f32 v5, v76, v77
	v_cvt_pk_f16_f32 v4, v74, v75
	s_waitcnt vmcnt(0)
	s_barrier
	global_store_dwordx2 v[2:3], v[4:5], off
	v_cvt_pk_f16_f32 v5, v84, v85
	v_cvt_pk_f16_f32 v4, v82, v83
	global_store_dwordx2 v[2:3], v[4:5], off offset:16
	v_cvt_pk_f16_f32 v5, v88, v89
	v_cvt_pk_f16_f32 v4, v86, v87
	global_store_dwordx2 v[2:3], v[4:5], off offset:32
	v_cvt_pk_f16_f32 v5, v110, v111
	v_cvt_pk_f16_f32 v4, v94, v95
	global_store_dwordx2 v[2:3], v[4:5], off offset:48
	v_cvt_pk_f16_f32 v5, v106, v107
	v_cvt_pk_f16_f32 v4, v108, v109
	global_store_dwordx2 v[2:3], v[4:5], off offset:64
	v_cvt_pk_f16_f32 v5, v100, v101
	v_cvt_pk_f16_f32 v4, v104, v105
	global_store_dwordx2 v[2:3], v[4:5], off offset:80
	v_cvt_pk_f16_f32 v5, v92, v93
	v_cvt_pk_f16_f32 v4, v96, v97
	global_store_dwordx2 v[2:3], v[4:5], off offset:96
	v_cvt_pk_f16_f32 v5, v102, v103
	v_cvt_pk_f16_f32 v4, v90, v91
	s_movk_i32 s0, 0x270
	global_store_dwordx2 v[2:3], v[4:5], off offset:112
	v_cmp_gt_u32_e32 vcc, s0, v0
	v_lshl_add_u32 v2, v0, 2, 0
	s_and_saveexec_b64 s[0:1], vcc
	ds_write_b32 v2, v159 offset:61440
	s_or_b64 exec, exec, s[0:1]
	s_movk_i32 s0, 0x70
	v_cmp_gt_u32_e32 vcc, s0, v0
	s_and_saveexec_b64 s[0:1], vcc
	ds_write_b32 v2, v161 offset:63488
	s_or_b64 exec, exec, s[0:1]
	s_cmpk_lt_u32 s14, 0x900
	s_cbranch_scc0 .LBB2_93
	s_lshl_b32 s0, s22, 10
	s_add_i32 s15, s22, -8
	s_add_i32 s0, s0, 0
	s_add_i32 s18, s0, 0x6000
	s_lshl_b64 s[0:1], s[14:15], 4
	s_and_b32 s1, s1, 15
	s_and_b32 s0, s0, 0xfffffc00
	s_add_u32 s0, s16, s0
	s_addc_u32 s1, s17, s1
	v_lshl_add_u64 v[2:3], v[120:121], 1, s[0:1]
	s_mov_b64 s[0:1], 0x36000
	v_lshl_add_u64 v[2:3], v[2:3], 0, s[0:1]
	s_mov_b64 s[0:1], 0x2000
